# v103 + P3 step barrier replaced by a per-parity-group (4-wave) LDS arrival-counter barrier; full s_barrier kept at the unit epilogue
# speedup vs baseline: 1.0131x; 1.0131x over previous
; #define LAS __attribute__((address_space(3)))
; __device__ __forceinline__ int lane_id() { int l; asm volatile("s_nop 4\n\tv_mbcnt_lo_u32_b32 %0, -1, 0\n\tv_mbcnt_hi_u32_b32 %0, -1, %0\n\ts_nop 4" : "=v"(l)); return l; }
; __device__ __forceinline__ void attn_phase_mfma(Frame& F) {
;     int tid = F.wave * 64 + lane_id(); asm volatile("" : "+v"(tid));
;     const int lane = tid & 63, wave = F.wave, grp = wave >> 2, hr = wave & 3, c = lane & 31, hh = lane >> 5, tg = tid & 255;
;     LAS unsigned char* KB0 = F.lds + RING_OFF + AT_KBUF + grp * (2 * 32 * AT_KPITCH);
;     LAS unsigned char* VB0 = F.lds + RING_OFF + AT_VBUF + grp * (2 * 128 * AT_VPITCH);
;     const LAS float* LUT = (const LAS float*)(F.lds + LUT_OFF);
;     LAS float* MG = (LAS float*)(F.lds + RING_OFF + AT_MERGE) + hr * (66 * 64);
;     const float C1 = 0.08838834764831845f * 1.4426950408889634f;
;     __syncthreads();
;     bf16* YA = F.Y + (size_t)2 * M * 1024;
;     const unsigned* maskw = (const unsigned*)F.MASK;
;     for (int rep = 0; rep < 2; ++rep) {
;         const int j = blockIdx.x, bg = j >> 5, i = j & 31, qb = rep == 0 ? 63 - i : i, b = bg >> 1, g = bg & 1, h = 4 * g + hr;
;         const int q0 = qb * 32, tq = q0 + c; const size_t row_q = (size_t)(b * SEQ + tq);
;         bf16x8 qf[8];
; #pragma unroll
;         for (int ks = 0; ks < 8; ++ks) qf[ks] = *(const bf16x8*)(F.PROJ + row_q * INWP + O_Q + h * HD + 16 * ks + 8 * hh);
;         f32x16 o[4];
; #pragma unroll
;         for (int db = 0; db < 4; ++db)
; #pragma unroll
;             for (int r = 0; r < 16; ++r) o[db][r] = 0.f;
;         float m = -INFINITY, l = 0.f;
;         const float bfar = LUT[h * 132 + 128];
;         const int nsteps = (qb + 2) >> 1;
;         const bf16* kvb = F.PROJ + (size_t)(b * SEQ) * INWP + g * HD;
;         v4u sk[2], sv[2]; unsigned mw = 0u, mwn = 0u;
;     ...
;         if (grp <= qb) { AT_LOAD_TILE(grp); AT_WRITE_TILE(0); mw = mwn; }
;         if (grp + 2 <= qb) AT_LOAD_TILE(grp + 2);
;         asm volatile("s_waitcnt lgkmcnt(0)" ::: "memory"); __builtin_amdgcn_s_barrier(); asm volatile("" ::: "memory");
.LBB0_540:
	v_readlane_b32 s0, v255, 42
	s_add_i32 s0, s0, 3
	v_readlane_b32 s4, v251, 14
	v_readlane_b32 s5, v251, 15
	s_cmp_le_i32 s4, s0
	s_cselect_b64 s[2:3], -1, 0
	s_cmp_lt_i32 s0, s5
	s_cselect_b64 s[4:5], -1, 0
	s_and_b64 s[2:3], s[2:3], s[4:5]
	s_andn2_b64 vcc, exec, s[2:3]
	s_cbranch_vccnz .LBB0_620
	v_readlane_b32 s0, v253, 16
	s_waitcnt vmcnt(1)
	s_nop 4
	v_mbcnt_lo_u32_b32 v0, -1, 0
	v_mbcnt_hi_u32_b32 v0, -1, v0
	s_nop 4
	v_readlane_b32 s2, v253, 30
	v_readlane_b32 s1, v255, 0
	v_add_u32_e32 v8, s0, v0
	v_readlane_b32 s0, v253, 19
	v_lshlrev_b32_e32 v0, 1, v8
	v_and_b32_e32 v9, 30, v0
	v_lshrrev_b32_e32 v0, 1, v8
	v_and_b32_e32 v220, 31, v8
	v_bfe_u32 v2, v8, 5, 1
	s_waitcnt vmcnt(0)
	v_and_b32_e32 v7, 0x78, v0
	v_lshlrev_b32_e32 v0, 4, v8
	v_and_b32_e32 v0, 0xf0, v0
	v_mul_u32_u24_e32 v4, 0x110, v220
	v_lshlrev_b32_e32 v5, 4, v2
	v_and_b32_e32 v1, 63, v8
	v_add_u32_e32 v10, s0, v0
	v_add3_u32 v221, s0, v4, v5
	v_readlane_b32 s0, v253, 21
	v_bfe_u32 v12, v8, 4, 4
	v_lshlrev_b32_e32 v3, 2, v8
	v_or_b32_e32 v11, s2, v9
	v_lshl_add_u32 v223, v1, 2, s0
	s_movk_i32 s0, 0x110
	v_or_b32_e32 v16, s2, v12
	v_readlane_b32 s2, v253, 39
	v_lshlrev_b32_e32 v192, 3, v2
	v_and_b32_e32 v3, 60, v3
	v_lshlrev_b32_e32 v222, 2, v2
	v_mad_u32_u24 v224, v12, s0, v10
	v_mul_u32_u24_e32 v2, 0x48, v7
	v_readlane_b32 s0, v253, 20
	v_readlane_b32 s3, v253, 40
	v_readlane_b32 s4, v253, 36
	v_or_b32_e32 v1, s1, v12
	v_add3_u32 v225, s0, v2, v3
	v_mov_b64_e32 v[2:3], s[2:3]
	v_readlane_b32 s5, v253, 37
	v_or_b32_e32 v13, 16, v1
	v_mad_u64_u32 v[4:5], s[2:3], v1, s94, v[2:3]
	v_mov_b32_e32 v1, v193
	v_lshl_add_u64 v[176:177], s[4:5], 0, v[192:193]
	v_lshl_add_u64 v[4:5], v[4:5], 0, v[0:1]
	s_mov_b64 s[4:5], 0x2800
	v_lshl_add_u64 v[178:179], v[4:5], 0, s[4:5]
	v_mad_u64_u32 v[4:5], s[2:3], v13, s94, v[2:3]
	v_or_b32_e32 v6, s1, v9
	v_lshl_add_u64 v[4:5], v[4:5], 0, v[0:1]
	v_or_b32_e32 v14, 1, v6
	v_lshl_add_u64 v[180:181], v[4:5], 0, s[4:5]
	v_mad_u64_u32 v[4:5], s[2:3], v6, s94, v[2:3]
	v_lshlrev_b32_e32 v6, 1, v7
	v_mov_b32_e32 v7, v193
	v_lshl_add_u64 v[4:5], v[4:5], 0, v[6:7]
	s_mov_b64 s[6:7], 0x2a00
	v_lshl_add_u64 v[182:183], v[4:5], 0, s[6:7]
	v_mad_u64_u32 v[4:5], s[2:3], v14, s94, v[2:3]
	v_lshl_add_u64 v[4:5], v[4:5], 0, v[6:7]
	v_lshl_add_u64 v[184:185], v[4:5], 0, s[6:7]
	v_mad_u64_u32 v[4:5], s[2:3], v16, s94, v[2:3]
	v_or_b32_e32 v17, 16, v16
	v_lshl_add_u64 v[4:5], v[4:5], 0, v[0:1]
	v_lshl_add_u64 v[186:187], v[4:5], 0, s[4:5]
	v_mad_u64_u32 v[4:5], s[2:3], v17, s94, v[2:3]
	v_lshl_add_u64 v[0:1], v[4:5], 0, v[0:1]
	v_lshl_add_u64 v[188:189], v[0:1], 0, s[4:5]
	v_mad_u64_u32 v[0:1], s[2:3], v11, s94, v[2:3]
	v_or_b32_e32 v18, 1, v11
	v_lshl_add_u64 v[0:1], v[0:1], 0, v[6:7]
	v_mul_u32_u24_e32 v19, 0x48, v220
	v_lshl_add_u64 v[190:191], v[0:1], 0, s[6:7]
	v_mad_u64_u32 v[0:1], s[2:3], v18, s94, v[2:3]
	v_lshl_add_u64 v[0:1], v[0:1], 0, v[6:7]
	v_add3_u32 v226, s0, v192, v19
	v_readlane_b32 s0, v254, 55
	v_lshl_add_u64 v[200:201], v[0:1], 0, s[6:7]
	v_readlane_b32 s4, v254, 56
	v_add_u32_e32 v0, s0, v220
	v_readlane_b32 s0, v254, 57
	v_readlane_b32 s1, v254, 58
	v_sub_u32_e32 v227, v0, v222
	v_add_u32_e32 v2, s4, v9
	v_mov_b64_e32 v[0:1], s[0:1]
	v_mad_u64_u32 v[0:1], s[2:3], v2, s94, v[0:1]
	v_lshlrev_b32_e32 v2, 4, v12
	v_mov_b32_e32 v3, v193
	v_readlane_b32 s0, v255, 1
	v_lshl_add_u64 v[202:203], v[0:1], 0, v[2:3]
	v_and_b32_e32 v4, 15, v8
	v_add_u32_e32 v2, s0, v12
	v_readlane_b32 s0, v254, 59
	v_readlane_b32 s1, v254, 60
	v_lshlrev_b32_e32 v4, 4, v4
	v_mov_b32_e32 v5, v193
	v_mov_b64_e32 v[0:1], s[0:1]
	v_mad_u64_u32 v[2:3], s[2:3], v2, s94, v[0:1]
	v_lshl_add_u64 v[204:205], v[2:3], 0, v[4:5]
	v_add_u32_e32 v2, s4, v12
	v_mul_u32_u24_e32 v15, 0x110, v12
	v_mad_u64_u32 v[0:1], s[2:3], v2, s94, v[0:1]
	v_lshl_add_u64 v[206:207], v[0:1], 0, v[4:5]
	s_mov_b64 s[2:3], -1
	v_lshlrev_b32_e32 v192, 1, v192
	v_add_u32_e32 v228, v10, v15
	s_mov_b32 s101, 0
	v_mov_b32_e32 v197, 0x1f000
	v_mov_b32_e32 v196, 0
	ds_write2_b32 v197, v196, v196 offset1:64
	v_readlane_b32 s36, v253, 16
	s_bfe_u32 s36, s36, 0x10008
	s_lshl_b32 s36, s36, 8
	s_add_i32 s36, s36, 0x1f000
	v_mov_b32_e32 v197, s36
	s_waitcnt lgkmcnt(0)
	s_barrier
	s_branch .LBB0_543

; __device__ __forceinline__ void attn_phase_mfma(Frame& F) {
;     ...
;             if (kt + 2 <= qb) { AT_WRITE_TILE((st + 1) & 1); mw = mwn; }
;             if (kt + 4 <= qb) AT_LOAD_TILE(kt + 4);
;             asm volatile("s_waitcnt lgkmcnt(0)" ::: "memory"); __builtin_amdgcn_s_barrier(); asm volatile("" ::: "memory");
;         }
.LBB0_559:
	s_waitcnt lgkmcnt(0)
	s_add_i32 s101, s101, 4
	s_mov_b64 s[36:37], exec
	s_mov_b64 exec, 1
	v_mov_b32_e32 v196, 1
	ds_add_u32 v197, v196
.Lp3g_spin:
	ds_read_b32 v196, v197
	s_waitcnt lgkmcnt(0)
	v_readfirstlane_b32 s0, v196
	s_cmp_lt_u32 s0, s101
	s_cbranch_scc1 .Lp3g_spin
	s_mov_b64 exec, s[36:37]
	s_sub_i32 s14, s14, 64
	s_add_i32 s17, s17, 1
	s_add_i32 s0, s13, s14
	s_add_i32 s16, s16, 64
	s_mov_b64 s[2:3], 0xd8000
	s_add_i32 s15, s15, 2
	v_lshl_add_u64 v[212:213], v[212:213], 0, 8
	v_lshl_add_u64 v[218:219], v[218:219], 0, s[2:3]
	v_lshl_add_u64 v[216:217], v[216:217], 0, s[2:3]
	s_cmp_eq_u32 s0, 0
	v_lshl_add_u64 v[214:215], v[214:215], 0, s[2:3]
	s_cbranch_scc1 .LBB0_563
	v_mov_b32_e32 v234, v232
	s_and_b32 s18, s17, 1
	s_cmp_gt_u32 s15, s10
	s_cbranch_scc1 .LBB0_555
	s_branch .LBB0_550

; __device__ __forceinline__ void attn_phase_mfma(Frame& F) {
;     ...
;             asm volatile("s_waitcnt lgkmcnt(0)" ::: "memory"); __builtin_amdgcn_s_barrier(); asm volatile("" ::: "memory");
;         }
;     ...
;         if (grp == 1) {
; #pragma unroll
;             for (int db = 0; db < 4; ++db)
; #pragma unroll
;                 for (int r = 0; r < 16; ++r) MG[(db * 16 + r) * 64 + lane] = o[db][r];
;             MG[64 * 64 + lane] = m; MG[65 * 64 + lane] = l;
;         }
.LBB0_563:
	s_waitcnt lgkmcnt(0)
	s_barrier
	v_readlane_b32 s0, v253, 32
	v_readlane_b32 s1, v253, 33
	s_andn2_b64 vcc, exec, s[0:1]
	s_cbranch_vccnz .LBB0_565
	ds_write2st64_b32 v223, v48, v49 offset1:1
	ds_write2st64_b32 v223, v50, v51 offset0:2 offset1:3
	ds_write2st64_b32 v223, v52, v53 offset0:4 offset1:5
	ds_write2st64_b32 v223, v54, v55 offset0:6 offset1:7
	ds_write2st64_b32 v223, v56, v57 offset0:8 offset1:9
	ds_write2st64_b32 v223, v58, v59 offset0:10 offset1:11
	ds_write2st64_b32 v223, v60, v61 offset0:12 offset1:13
	ds_write2st64_b32 v223, v62, v63 offset0:14 offset1:15
	ds_write2st64_b32 v223, v32, v33 offset0:16 offset1:17
	ds_write2st64_b32 v223, v34, v35 offset0:18 offset1:19
	ds_write2st64_b32 v223, v36, v37 offset0:20 offset1:21
	ds_write2st64_b32 v223, v38, v39 offset0:22 offset1:23
	ds_write2st64_b32 v223, v40, v41 offset0:24 offset1:25
	ds_write2st64_b32 v223, v42, v43 offset0:26 offset1:27
	ds_write2st64_b32 v223, v44, v45 offset0:28 offset1:29
	ds_write2st64_b32 v223, v46, v47 offset0:30 offset1:31
	ds_write2st64_b32 v223, v16, v17 offset0:32 offset1:33
	ds_write2st64_b32 v223, v18, v19 offset0:34 offset1:35
	ds_write2st64_b32 v223, v20, v21 offset0:36 offset1:37
	ds_write2st64_b32 v223, v22, v23 offset0:38 offset1:39
	ds_write2st64_b32 v223, v24, v25 offset0:40 offset1:41
	ds_write2st64_b32 v223, v26, v27 offset0:42 offset1:43
	ds_write2st64_b32 v223, v28, v29 offset0:44 offset1:45
	ds_write2st64_b32 v223, v30, v31 offset0:46 offset1:47
	ds_write2st64_b32 v223, v0, v1 offset0:48 offset1:49
	ds_write2st64_b32 v223, v2, v3 offset0:50 offset1:51
	ds_write2st64_b32 v223, v4, v5 offset0:52 offset1:53
	ds_write2st64_b32 v223, v6, v7 offset0:54 offset1:55
	ds_write2st64_b32 v223, v8, v9 offset0:56 offset1:57
	ds_write2st64_b32 v223, v10, v11 offset0:58 offset1:59
	ds_write2st64_b32 v223, v12, v13 offset0:60 offset1:61
	ds_write2st64_b32 v223, v14, v15 offset0:62 offset1:63
	ds_write2st64_b32 v223, v232, v210 offset0:64 offset1:65
